# speedup vs baseline: 1.0150x; 1.0061x over previous
.Lmk_p72:
	v_bfe_u32 v121, v121, 16, 4
	v_mov_b64_e32 v[130:131], 0
	v_mov_b64_e32 v[132:133], 0
	v_mov_b64_e32 v[134:135], 0
	v_mov_b64_e32 v[136:137], 0
	v_mov_b64_e32 v[138:139], 0
	v_mov_b64_e32 v[140:141], 0
	v_mov_b64_e32 v[142:143], 0
	v_mov_b64_e32 v[144:145], 0
	v_and_b32_e32 v200, 1, v114
	v_cmp_eq_u32_e32 vcc, 1, v200
	s_nop 1
	v_cndmask_b32_e32 v124, v124, v174, vcc
	v_mov_b64_e32 v[168:169], s[12:13]
	v_mov_b64_e32 v[170:171], s[12:13]
	v_xor_b32_e32 v117, 64, v122
	s_mov_b32 s30, s85
	s_lshl_b32 s6, s43, 6
	s_sub_i32 s83, s44, s6
	s_lshl_b32 s6, s43, 8
	s_add_i32 s82, s78, s6
	s_mov_b32 s66, s41
	s_branch .LBB2_62

.LBB2_64:
	v_cmp_gt_i32_e64 s[56:57], s66, v110
	v_lshl_add_u32 v115, v121, 1, v191
	v_lshl_add_u32 v34, v121, 2, s86
	ds_bpermute_b32 v121, v34, v197
	s_cmp_lt_i32 s66, 33
	s_cbranch_scc1 .Lmk_half_iter
	ds_read_b128 v[208:211], v122
	ds_read_b128 v[212:215], v117
	ds_read_b128 v[216:219], v122 offset:2048
	ds_read_b128 v[220:223], v117 offset:2048
	ds_read_b128 v[224:227], v122 offset:4096
	ds_read_b128 v[228:231], v117 offset:4096
	ds_read_b128 v[232:235], v122 offset:6144
	ds_read_b128 v[236:239], v117 offset:6144
	ds_read_b64_tr_b16 v[130:131], v186 offset:0
	ds_read_b64_tr_b16 v[132:133], v186 offset:2048
	ds_read_b64_tr_b16 v[134:135], v188 offset:0
	ds_read_b64_tr_b16 v[136:137], v188 offset:2048
	ds_read_b64_tr_b16 v[138:139], v189 offset:0
	ds_read_b64_tr_b16 v[140:141], v189 offset:2048
	ds_read_b64_tr_b16 v[142:143], v190 offset:0
	ds_read_b64_tr_b16 v[144:145], v190 offset:2048
.Lmk_ua_ready:
	s_waitcnt lgkmcnt(8)
	v_mfma_f32_16x16x32_f16 v[200:203], v[240:243], v[208:211], 0
	v_mfma_f32_16x16x32_f16 v[160:163], v[240:243], v[216:219], 0
	v_mfma_f32_16x16x32_f16 v[248:251], v[240:243], v[224:227], 0
	v_mfma_f32_16x16x32_f16 v[252:255], v[240:243], v[232:235], 0
	v_mfma_f32_16x16x32_f16 v[200:203], v[244:247], v[212:215], v[200:203]
	v_mfma_f32_16x16x32_f16 v[160:163], v[244:247], v[220:223], v[160:163]
	v_mfma_f32_16x16x32_f16 v[248:251], v[244:247], v[228:231], v[248:251]
	v_mfma_f32_16x16x32_f16 v[252:255], v[244:247], v[236:239], v[252:255]
	ds_read_b64_tr_b16 v[146:147], v186 offset:4096
	ds_read_b64_tr_b16 v[148:149], v186 offset:6144
	ds_read_b64_tr_b16 v[150:151], v188 offset:4096
	ds_read_b64_tr_b16 v[152:153], v188 offset:6144
	ds_read_b64_tr_b16 v[154:155], v189 offset:4096
	ds_read_b64_tr_b16 v[156:157], v189 offset:6144
	ds_read_b64_tr_b16 v[204:205], v190 offset:4096
	ds_read_b64_tr_b16 v[206:207], v190 offset:6144
	v_cndmask_b32_e64 v34, v200, v160, s[60:61]
	v_cndmask_b32_e64 v34, v34, v248, s[62:63]
	v_cndmask_b32_e64 v34, v34, v252, s[64:65]
.Lmk_half_join:
	v_add_f32_e32 v34, v34, v121
	v_mul_f32_e32 v121, 0x3e4ccccd, v34
	v_max_f32_e32 v34, v34, v121
	v_cmp_gt_f32_e32 vcc, v34, v184
	s_and_b64 s[68:69], s[56:57], vcc
	s_cmp_eq_u64 s[68:69], 0
	s_cbranch_scc0 .Lmk_max
	v_add_u32_e32 v229, s82, v172
	v_add_u32_e32 v230, s82, v173
	ds_read_u16 v224, v229 offset:0
	ds_read_u16 v225, v229 offset:32
	ds_read_u16 v226, v229 offset:64
	ds_read_u16 v227, v229 offset:96
	ds_read_u16 v232, v229 offset:128
	ds_read_u16 v233, v229 offset:160
	ds_read_u16 v234, v229 offset:192
	ds_read_u16 v235, v229 offset:224
	v_bfe_u32 v121, v183, 16, 4
	ds_read_b32 v183, v230
.Lmk_nomax:
	v_sub_f32_e32 v34, v34, v195
	v_fmamk_f32 v34, v34, 0x3fb8aa3b, v187
	v_exp_f32_e32 v34, v34
	s_nop 0
	v_cvt_f16_f32_e32 v34, v34
	v_cndmask_b32_e64 v34, 0, v34, s[56:57]
	ds_write_b16 v115, v34
	ds_read_b64_tr_b16 v[200:201], v193 offset:0
	ds_read_b64_tr_b16 v[202:203], v193 offset:512
	ds_read_b64_tr_b16 v[160:161], v193 offset:1024
	ds_read_b64_tr_b16 v[162:163], v193 offset:1536
	s_and_b64 vcc, exec, s[54:55]
	s_cbranch_vccnz .Lmk_first_path
	s_waitcnt vmcnt(0)
	s_waitcnt lgkmcnt(0)
	v_mfma_f32_16x16x32_f16 v[54:57], v[130:133], v[200:203], v[54:57]
	ds_write_b16 v115, v35
	ds_write_b128 v196, v[10:13]
	v_mfma_f32_16x16x32_f16 v[58:61], v[134:137], v[200:203], v[58:61]
	ds_write_b128 v196, v[14:17] offset:1024
	v_mfma_f32_16x16x32_f16 v[62:65], v[138:141], v[200:203], v[62:65]
	ds_write_b128 v196, v[30:33] offset:2048
	v_mfma_f32_16x16x32_f16 v[66:69], v[142:145], v[200:203], v[66:69]
	ds_write_b128 v196, v[26:29] offset:3072
	v_mfma_f32_16x16x32_f16 v[70:73], v[168:171], v[200:203], v[70:73]

.Lmk_max:
	v_cndmask_b32_e64 v161, v185, v34, s[56:57]
	s_nop 1
	v_max_f32_dpp v161, v161, v161 row_shr:1 row_mask:0xf bank_mask:0xf
	v_bfe_u32 v121, v183, 16, 4
	s_nop 0
	v_max_f32_dpp v161, v161, v161 row_shr:2 row_mask:0xf bank_mask:0xf
	v_add_u32_e32 v229, s82, v172
	v_add_u32_e32 v230, s82, v173
	v_max_f32_dpp v161, v161, v161 row_shr:4 row_mask:0xf bank_mask:0xf
	ds_read_u16 v224, v229 offset:0
	ds_read_u16 v225, v229 offset:32
	v_max_f32_dpp v161, v161, v161 row_shr:8 row_mask:0xf bank_mask:0xf
	ds_read_u16 v226, v229 offset:64
	ds_read_u16 v227, v229 offset:96
	v_max_f32_dpp v161, v161, v161 row_bcast:15 row_mask:0xa bank_mask:0xf
	ds_read_u16 v232, v229 offset:128
	ds_read_u16 v233, v229 offset:160
	v_max_f32_dpp v161, v161, v161 row_bcast:31 row_mask:0xc bank_mask:0xf
	ds_read_u16 v234, v229 offset:192
	ds_read_u16 v235, v229 offset:224
	v_readlane_b32 s70, v161, 63
	ds_read_b32 v183, v230
	s_and_b64 vcc, exec, s[54:55]
	s_nop 0
	v_mov_b32_e32 v161, s70
	s_cbranch_vccz .Lmk_rescale
.Lmk_norescale:
	v_mov_b32_e32 v195, v161
	v_add_f32_e32 v184, 0x40200000, v161
	s_branch .Lmk_nomax

.Lmk_half_iter:
	s_cmp_lt_i32 s66, 17
	s_cbranch_scc1 .Lmk_quarter_iter
	ds_read_b128 v[208:211], v122
	ds_read_b128 v[212:215], v117
	ds_read_b128 v[216:219], v122 offset:2048
	ds_read_b128 v[220:223], v117 offset:2048
	ds_read_b64_tr_b16 v[130:131], v186 offset:0
	ds_read_b64_tr_b16 v[132:133], v186 offset:2048
	ds_read_b64_tr_b16 v[134:135], v188 offset:0
	ds_read_b64_tr_b16 v[136:137], v188 offset:2048
	ds_read_b64_tr_b16 v[138:139], v189 offset:0
	ds_read_b64_tr_b16 v[140:141], v189 offset:2048
	ds_read_b64_tr_b16 v[142:143], v190 offset:0
	ds_read_b64_tr_b16 v[144:145], v190 offset:2048
	s_waitcnt lgkmcnt(8)
	v_mfma_f32_16x16x32_f16 v[200:203], v[240:243], v[208:211], 0
	v_mfma_f32_16x16x32_f16 v[160:163], v[240:243], v[216:219], 0
	v_mfma_f32_16x16x32_f16 v[200:203], v[244:247], v[212:215], v[200:203]
	v_mfma_f32_16x16x32_f16 v[160:163], v[244:247], v[220:223], v[160:163]
	s_nop 7
	v_cndmask_b32_e64 v34, v200, v160, s[60:61]
	s_branch .Lmk_half_join
.Lmk_quarter_iter:
	ds_read_b128 v[208:211], v122
	ds_read_b128 v[212:215], v117
	ds_read_b64_tr_b16 v[130:131], v186 offset:0
	ds_read_b64_tr_b16 v[134:135], v188 offset:0
	ds_read_b64_tr_b16 v[138:139], v189 offset:0
	ds_read_b64_tr_b16 v[142:143], v190 offset:0
	s_waitcnt lgkmcnt(4)
	v_mfma_f32_16x16x32_f16 v[200:203], v[240:243], v[208:211], 0
	v_mfma_f32_16x16x32_f16 v[200:203], v[244:247], v[212:215], v[200:203]
	s_nop 7
	v_mov_b32_e32 v34, v200
	s_branch .Lmk_half_join

.LBB2_93:
	v_mov_b32_e32 v184, v185
	s_lshl_b32 s0, s50, 7
	s_add_i32 s0, s0, 0x26000
	v_lshl_add_u32 v36, v107, 4, s0
	ds_read_b128 v[240:243], v36
	ds_read_b128 v[244:247], v36 offset:64
	s_cmp_gt_i32 s50, 35
	v_mov_b32_e32 v125, 0
	s_cbranch_scc1 .LBB2_103
	v_mov_b32_dpp v174, v124 quad_perm:[1,1,1,1] row_mask:0xf bank_mask:0xf
	v_mov_b32_dpp v124, v124 quad_perm:[0,0,0,0] row_mask:0xf bank_mask:0xf
	v_sub_u32_e32 v125, v174, v124
	s_add_i32 s0, s50, 2
	v_mov_b32_e32 v74, 0
	v_cndmask_b32_e64 v34, 0, v125, s[2:3]
	s_mul_i32 s0, s0, 0xc3500
	v_lshl_add_u32 v36, v124, 2, v118
	v_add_u32_dpp v34, v34, v34 row_shr:1 row_mask:0xf bank_mask:0xf bound_ctrl:1
	s_add_u32 s0, s90, s0
	s_addc_u32 s1, s91, 0
	v_add_u32_dpp v34, v34, v34 row_shr:2 row_mask:0xf bank_mask:0xf bound_ctrl:1
	v_mov_b32_e32 v120, v124
	s_nop 0
	v_add_u32_dpp v34, v34, v34 row_shr:4 row_mask:0xf bank_mask:0xf bound_ctrl:1
	global_load_dwordx4 v[164:167], v36, s[0:1]
	s_nop 0
	v_add_u32_dpp v34, v34, v34 row_shr:8 row_mask:0xf bank_mask:0xf bound_ctrl:1
	s_nop 1
	v_add_u32_dpp v34, v34, v34 row_bcast:15 row_mask:0xa bank_mask:0xf
	s_nop 1
	v_mov_b32_dpp v74, v34 row_bcast:31 row_mask:0xc bank_mask:0xf
	v_sub_u32_e32 v36, v74, v125
	v_add_u32_e32 v129, v36, v34
	v_sub_u32_e32 v36, 0x2f0, v129
	v_min_i32_e32 v125, v125, v36
